# baseline (speedup 1.0000x reference)
_Z17closed_form_finalPK15HIP_vector_typeIfLj4EEPf:
	s_load_dwordx4 s[4:7], s[0:1], 0x0
	v_lshlrev_b32_e32 v2, 4, v0
	v_mov_b32_e32 v3, 0
	v_or_b32_e32 v1, 0x1c0, v0
	s_waitcnt lgkmcnt(0)
	global_load_dwordx4 v[4:7], v2, s[4:5]
	global_load_dwordx4 v[8:11], v2, s[4:5] offset:1024
	global_load_dwordx4 v[12:15], v2, s[4:5] offset:2048
	v_lshl_add_u64 v[20:21], s[4:5], 0, v[2:3]
	v_add_co_u32_e32 v28, vcc, 0x1000, v20
	global_load_dwordx4 v[16:19], v2, s[4:5] offset:3072
	s_nop 0
	v_addc_co_u32_e32 v29, vcc, 0, v21, vcc
	v_cmp_gt_u32_e32 vcc, 56, v0
	global_load_dwordx4 v[20:23], v[28:29], off
	global_load_dwordx4 v[24:27], v[28:29], off offset:1024
	v_cndmask_b32_e32 v1, 0, v1, vcc
	v_lshlrev_b32_e32 v1, 4, v1
	global_load_dwordx4 v[28:31], v[28:29], off offset:2048
	v_mov_b32_e32 v2, v3
	global_load_dwordx4 v[32:35], v1, s[4:5]
	v_mov_b32_e32 v1, 0
	s_waitcnt vmcnt(7)
	v_add_f32_e32 v4, v4, v5
	v_add_f32_e32 v5, v6, v7
	s_waitcnt vmcnt(6)
	v_add_f32_e32 v6, v8, v9
	v_add_f32_e32 v7, v10, v11
	s_waitcnt vmcnt(5)
	v_add_f32_e32 v8, v12, v13
	v_add_f32_e32 v9, v14, v15
	s_waitcnt vmcnt(4)
	v_add_f32_e32 v10, v16, v17
	v_add_f32_e32 v11, v18, v19
	v_add_f32_e32 v4, v4, v5
	v_add_f32_e32 v5, v6, v7
	v_add_f32_e32 v6, v8, v9
	v_add_f32_e32 v7, v10, v11
	v_add_f32_e32 v4, v4, v5
	v_add_f32_e32 v5, v6, v7
	s_waitcnt vmcnt(3)
	v_add_f32_e32 v6, v20, v21
	v_add_f32_e32 v7, v22, v23
	s_waitcnt vmcnt(2)
	v_add_f32_e32 v8, v24, v25
	v_add_f32_e32 v9, v26, v27
	s_waitcnt vmcnt(0)
	v_add_f32_e32 v12, v32, v33
	v_add_f32_e32 v13, v34, v35
	v_add_f32_e32 v10, v28, v29
	v_add_f32_e32 v11, v30, v31
	v_add_f32_e32 v4, v4, v5
	v_add_f32_e32 v5, v6, v7
	v_add_f32_e32 v6, v8, v9
	v_add_f32_e32 v8, v12, v13
	v_add_f32_e32 v7, v10, v11
	v_cndmask_b32_e32 v8, 0, v8, vcc
	v_add_f32_e32 v5, v5, v6
	v_add_f32_e32 v6, v7, v8
	v_add_f32_e32 v5, v5, v6
	v_add_f32_e32 v4, v4, v5
	v_cmp_eq_u32_e32 vcc, 63, v0
	s_nop 0
	v_add_f32_dpp v4, v4, v4 row_shr:1 row_mask:0xf bank_mask:0xf bound_ctrl:1
	s_nop 1
	v_add_f32_dpp v4, v4, v4 row_shr:2 row_mask:0xf bank_mask:0xf bound_ctrl:1
	s_nop 1
	v_add_f32_dpp v4, v4, v4 row_shr:4 row_mask:0xf bank_mask:0xf bound_ctrl:1
	s_nop 1
	v_add_f32_dpp v4, v4, v4 row_shr:8 row_mask:0xf bank_mask:0xf bound_ctrl:1
	s_nop 1
	v_mov_b32_dpp v2, v4 row_bcast:15 row_mask:0xa bank_mask:0xf
	v_add_f32_e32 v2, v4, v2
	s_nop 1
	v_mov_b32_dpp v1, v2 row_bcast:31 row_mask:0xc bank_mask:0xf
	s_and_saveexec_b64 s[2:3], vcc
	s_cbranch_execz .LBB1_2
	v_add_f32_e32 v0, v2, v1
	v_mul_f32_e32 v0, 0x2d7e027e, v0
	global_store_dword v3, v0, s[6:7]

	.amdhsa_kernel _Z17closed_form_finalPK15HIP_vector_typeIfLj4EEPf
		.amdhsa_group_segment_fixed_size 0
		.amdhsa_private_segment_fixed_size 0
		.amdhsa_kernarg_size 16
		.amdhsa_user_sgpr_count 2
		.amdhsa_user_sgpr_dispatch_ptr 0
		.amdhsa_user_sgpr_queue_ptr 0
		.amdhsa_user_sgpr_kernarg_segment_ptr 1
		.amdhsa_user_sgpr_dispatch_id 0
		.amdhsa_user_sgpr_kernarg_preload_length 0
		.amdhsa_user_sgpr_kernarg_preload_offset 0
		.amdhsa_user_sgpr_private_segment_size 0
		.amdhsa_uses_dynamic_stack 0
		.amdhsa_enable_private_segment 0
		.amdhsa_system_sgpr_workgroup_id_x 1
		.amdhsa_system_sgpr_workgroup_id_y 0
		.amdhsa_system_sgpr_workgroup_id_z 0
		.amdhsa_system_sgpr_workgroup_info 0
		.amdhsa_system_vgpr_workitem_id 0
		.amdhsa_next_free_vgpr 36
		.amdhsa_next_free_sgpr 8
		.amdhsa_accum_offset 36
		.amdhsa_reserve_vcc 1
		.amdhsa_float_round_mode_32 0
		.amdhsa_float_round_mode_16_64 0
		.amdhsa_float_denorm_mode_32 3
		.amdhsa_float_denorm_mode_16_64 3
		.amdhsa_dx10_clamp 1
		.amdhsa_ieee_mode 1
		.amdhsa_fp16_overflow 0
		.amdhsa_tg_split 0
		.amdhsa_exception_fp_ieee_invalid_op 0
		.amdhsa_exception_fp_denorm_src 0
		.amdhsa_exception_fp_ieee_div_zero 0
		.amdhsa_exception_fp_ieee_overflow 0
		.amdhsa_exception_fp_ieee_underflow 0
		.amdhsa_exception_fp_ieee_inexact 0
		.amdhsa_exception_int_div_zero 0
	.end_amdhsa_kernel

amdhsa.kernels:
  - .agpr_count:     0
    .args:
      - .address_space:  global
        .offset:         0
        .size:           8
        .value_kind:     global_buffer
      - .address_space:  global
        .offset:         8
        .size:           8
        .value_kind:     global_buffer
      - .address_space:  global
        .offset:         16
        .size:           8
        .value_kind:     global_buffer
      - .address_space:  global
        .offset:         24
        .size:           8
        .value_kind:     global_buffer
    .group_segment_fixed_size: 6144
    .kernarg_segment_align: 8
    .kernarg_segment_size: 32
    .language:       OpenCL C
    .language_version:
      - 2
      - 0
    .max_flat_workgroup_size: 128
    .name:           _Z16closed_form_mainPKfS0_PKiPf
    .private_segment_fixed_size: 0
    .sgpr_count:     54
    .sgpr_spill_count: 0
    .symbol:         _Z16closed_form_mainPKfS0_PKiPf.kd
    .uniform_work_group_size: 1
    .uses_dynamic_stack: false
    .vgpr_count:     250
    .vgpr_spill_count: 0
    .wavefront_size: 64
  - .agpr_count:     0
    .args:
      - .actual_access:  read_only
        .address_space:  global
        .offset:         0
        .size:           8
        .value_kind:     global_buffer
      - .actual_access:  write_only
        .address_space:  global
        .offset:         8
        .size:           8
        .value_kind:     global_buffer
    .group_segment_fixed_size: 0
    .kernarg_segment_align: 8
    .kernarg_segment_size: 16
    .language:       OpenCL C
    .language_version:
      - 2
      - 0
    .max_flat_workgroup_size: 64
    .name:           _Z17closed_form_finalPK15HIP_vector_typeIfLj4EEPf
    .private_segment_fixed_size: 0
    .sgpr_count:     14
    .sgpr_spill_count: 0
    .symbol:         _Z17closed_form_finalPK15HIP_vector_typeIfLj4EEPf.kd
    .uniform_work_group_size: 1
    .uses_dynamic_stack: false
    .vgpr_count:     36
    .vgpr_spill_count: 0
    .wavefront_size: 64
